# accumulator-stationary MFMA order in 4 GEMM K-loops (k0,k1 of the same accumulator back to back), on top of v033
# speedup vs baseline: 1.0168x; 1.0157x over previous
.LBB0_114:
	ds_read_b128 v[130:133], v220
	ds_read_b128 v[134:137], v220 offset:1024
	ds_read_b128 v[138:141], v220 offset:2048
	ds_read_b128 v[142:145], v220 offset:3072
	ds_read_b128 v[146:149], v221
	ds_read_b128 v[150:153], v221 offset:1024
	ds_read_b128 v[154:157], v221 offset:2048
	ds_read_b128 v[158:161], v221 offset:3072
	s_add_i32 s46, s64, 0xfff80080
	s_cmp_eq_u32 s84, 28
	s_cselect_b32 s87, s62, s46
	s_cselect_b32 s86, s63, s65
	s_or_b32 s85, s87, 0x80
	s_mov_b32 m0, s93
	ds_read_b128 v[162:165], v222
	ds_read_b128 v[166:169], v222 offset:1024
	ds_read_b128 v[170:173], v222 offset:2048
	ds_read_b128 v[174:177], v222 offset:3072
	ds_read_b128 v[178:181], v222 offset:4096
	ds_read_b128 v[182:185], v222 offset:5120
	ds_read_b128 v[186:189], v222 offset:6144
	ds_read_b128 v[212:215], v222 offset:7168
	buffer_load_dwordx4 v1, s[40:43], s64 offen lds
	s_mov_b32 m0, s94
	s_nop 0
	buffer_load_dwordx4 v216, s[40:43], s64 offen lds
	s_waitcnt vmcnt(8)
	s_waitcnt lgkmcnt(0)
	s_barrier
	s_waitcnt lgkmcnt(7)
	v_mfma_f32_16x16x32_bf16 v[126:129], v[130:133], v[162:165], v[126:129]
	v_mfma_f32_16x16x32_bf16 v[126:129], v[134:137], v[166:169], v[126:129]
	s_waitcnt lgkmcnt(5)
	v_mfma_f32_16x16x32_bf16 v[122:125], v[138:141], v[162:165], v[122:125]
	v_mfma_f32_16x16x32_bf16 v[122:125], v[142:145], v[166:169], v[122:125]
	s_waitcnt lgkmcnt(3)
	v_mfma_f32_16x16x32_bf16 v[114:117], v[130:133], v[170:173], v[114:117]
	v_mfma_f32_16x16x32_bf16 v[114:117], v[134:137], v[174:177], v[114:117]
	s_waitcnt lgkmcnt(1)
	v_mfma_f32_16x16x32_bf16 v[106:109], v[138:141], v[170:173], v[106:109]
	v_mfma_f32_16x16x32_bf16 v[106:109], v[142:145], v[174:177], v[106:109]
	v_mfma_f32_16x16x32_bf16 v[102:105], v[130:133], v[178:181], v[102:105]
	v_mfma_f32_16x16x32_bf16 v[102:105], v[134:137], v[182:185], v[102:105]
	v_mfma_f32_16x16x32_bf16 v[94:97], v[138:141], v[178:181], v[94:97]
	v_mfma_f32_16x16x32_bf16 v[94:97], v[142:145], v[182:185], v[94:97]
	v_mfma_f32_16x16x32_bf16 v[86:89], v[130:133], v[186:189], v[86:89]
	v_mfma_f32_16x16x32_bf16 v[86:89], v[134:137], v[212:215], v[86:89]
	s_waitcnt lgkmcnt(0)
	v_mfma_f32_16x16x32_bf16 v[78:81], v[138:141], v[186:189], v[78:81]
	v_mfma_f32_16x16x32_bf16 v[78:81], v[142:145], v[212:215], v[78:81]
	v_mfma_f32_16x16x32_bf16 v[118:121], v[146:149], v[162:165], v[118:121]
	v_mfma_f32_16x16x32_bf16 v[118:121], v[150:153], v[166:169], v[118:121]
	v_mfma_f32_16x16x32_bf16 v[110:113], v[154:157], v[162:165], v[110:113]
	v_mfma_f32_16x16x32_bf16 v[110:113], v[158:161], v[166:169], v[110:113]
	v_mfma_f32_16x16x32_bf16 v[98:101], v[146:149], v[170:173], v[98:101]
	v_mfma_f32_16x16x32_bf16 v[98:101], v[150:153], v[174:177], v[98:101]
	v_mfma_f32_16x16x32_bf16 v[90:93], v[154:157], v[170:173], v[90:93]
	v_mfma_f32_16x16x32_bf16 v[90:93], v[158:161], v[174:177], v[90:93]
	v_mfma_f32_16x16x32_bf16 v[82:85], v[146:149], v[178:181], v[82:85]
	v_mfma_f32_16x16x32_bf16 v[82:85], v[150:153], v[182:185], v[82:85]
	v_mfma_f32_16x16x32_bf16 v[74:77], v[154:157], v[178:181], v[74:77]
	v_mfma_f32_16x16x32_bf16 v[74:77], v[158:161], v[182:185], v[74:77]
	v_mfma_f32_16x16x32_bf16 v[70:73], v[146:149], v[186:189], v[70:73]
	v_mfma_f32_16x16x32_bf16 v[70:73], v[150:153], v[212:215], v[70:73]
	v_mfma_f32_16x16x32_bf16 v[66:69], v[154:157], v[186:189], v[66:69]
	v_mfma_f32_16x16x32_bf16 v[66:69], v[158:161], v[212:215], v[66:69]
	s_barrier
	s_mov_b32 m0, s69
	s_mov_b32 s46, s42
	s_mov_b32 s47, s43
	ds_read_b128 v[162:165], v222 offset:16384
	ds_read_b128 v[166:169], v222 offset:17408
	ds_read_b128 v[170:173], v222 offset:18432
	ds_read_b128 v[174:177], v222 offset:19456
	ds_read_b128 v[178:181], v222 offset:20480
	ds_read_b128 v[182:185], v222 offset:21504
	ds_read_b128 v[186:189], v222 offset:22528
	ds_read_b128 v[212:215], v222 offset:23552
	buffer_load_dwordx4 v191, s[44:47], s86 offen lds
	s_mov_b32 m0, s70
	s_add_i32 s88, s86, 0x80000
	buffer_load_dwordx4 v217, s[44:47], s86 offen lds
	s_mov_b32 m0, s71
	s_nop 0
	buffer_load_dwordx4 v191, s[44:47], s88 offen lds
	s_mov_b32 m0, s72
	s_nop 0
	buffer_load_dwordx4 v217, s[44:47], s88 offen lds
	s_mov_b32 m0, s68
	s_nop 0
	buffer_load_dwordx4 v1, s[40:43], s87 offen lds
	s_mov_b32 m0, s73
	s_nop 0
	buffer_load_dwordx4 v216, s[40:43], s87 offen lds
	s_waitcnt vmcnt(8)
	s_waitcnt lgkmcnt(0)
	s_barrier
	s_waitcnt lgkmcnt(7)
	v_mfma_f32_16x16x32_bf16 v[62:65], v[130:133], v[162:165], v[62:65]
	v_mfma_f32_16x16x32_bf16 v[62:65], v[134:137], v[166:169], v[62:65]
	s_waitcnt lgkmcnt(5)
	v_mfma_f32_16x16x32_bf16 v[58:61], v[138:141], v[162:165], v[58:61]
	v_mfma_f32_16x16x32_bf16 v[58:61], v[142:145], v[166:169], v[58:61]
	s_waitcnt lgkmcnt(3)
	v_mfma_f32_16x16x32_bf16 v[54:57], v[130:133], v[170:173], v[54:57]
	v_mfma_f32_16x16x32_bf16 v[54:57], v[134:137], v[174:177], v[54:57]
	s_waitcnt lgkmcnt(1)
	v_mfma_f32_16x16x32_bf16 v[46:49], v[138:141], v[170:173], v[46:49]
	v_mfma_f32_16x16x32_bf16 v[46:49], v[142:145], v[174:177], v[46:49]
	v_mfma_f32_16x16x32_bf16 v[38:41], v[130:133], v[178:181], v[38:41]
	v_mfma_f32_16x16x32_bf16 v[38:41], v[134:137], v[182:185], v[38:41]
	v_mfma_f32_16x16x32_bf16 v[30:33], v[138:141], v[178:181], v[30:33]
	v_mfma_f32_16x16x32_bf16 v[30:33], v[142:145], v[182:185], v[30:33]
	v_mfma_f32_16x16x32_bf16 v[22:25], v[130:133], v[186:189], v[22:25]
	v_mfma_f32_16x16x32_bf16 v[22:25], v[134:137], v[212:215], v[22:25]
	s_waitcnt lgkmcnt(0)
	v_mfma_f32_16x16x32_bf16 v[14:17], v[138:141], v[186:189], v[14:17]
	v_mfma_f32_16x16x32_bf16 v[14:17], v[142:145], v[212:215], v[14:17]
	v_mfma_f32_16x16x32_bf16 v[50:53], v[146:149], v[162:165], v[50:53]
	v_mfma_f32_16x16x32_bf16 v[50:53], v[150:153], v[166:169], v[50:53]
	v_mfma_f32_16x16x32_bf16 v[42:45], v[154:157], v[162:165], v[42:45]
	v_mfma_f32_16x16x32_bf16 v[42:45], v[158:161], v[166:169], v[42:45]
	v_mfma_f32_16x16x32_bf16 v[34:37], v[146:149], v[170:173], v[34:37]
	v_mfma_f32_16x16x32_bf16 v[34:37], v[150:153], v[174:177], v[34:37]
	v_mfma_f32_16x16x32_bf16 v[26:29], v[154:157], v[170:173], v[26:29]
	v_mfma_f32_16x16x32_bf16 v[26:29], v[158:161], v[174:177], v[26:29]
	v_mfma_f32_16x16x32_bf16 v[18:21], v[146:149], v[178:181], v[18:21]
	v_mfma_f32_16x16x32_bf16 v[18:21], v[150:153], v[182:185], v[18:21]
	v_mfma_f32_16x16x32_bf16 v[10:13], v[154:157], v[178:181], v[10:13]
	v_mfma_f32_16x16x32_bf16 v[10:13], v[158:161], v[182:185], v[10:13]
	v_mfma_f32_16x16x32_bf16 v[6:9], v[146:149], v[186:189], v[6:9]
	v_mfma_f32_16x16x32_bf16 v[6:9], v[150:153], v[212:215], v[6:9]
	v_mfma_f32_16x16x32_bf16 v[2:5], v[154:157], v[186:189], v[2:5]
	v_mfma_f32_16x16x32_bf16 v[2:5], v[158:161], v[212:215], v[2:5]
	s_barrier
	ds_read_b128 v[130:133], v223
	ds_read_b128 v[134:137], v223 offset:1024
	ds_read_b128 v[138:141], v223 offset:2048
	ds_read_b128 v[142:145], v223 offset:3072
	ds_read_b128 v[146:149], v224
	ds_read_b128 v[150:153], v224 offset:1024
	ds_read_b128 v[154:157], v224 offset:2048
	ds_read_b128 v[158:161], v224 offset:3072
	s_add_i32 s87, s87, 0x80000
	s_mov_b32 m0, s74
	ds_read_b128 v[162:165], v222 offset:32768
	ds_read_b128 v[166:169], v222 offset:33792
	ds_read_b128 v[170:173], v222 offset:34816
	ds_read_b128 v[174:177], v222 offset:35840
	ds_read_b128 v[178:181], v222 offset:36864
	ds_read_b128 v[182:185], v222 offset:37888
	ds_read_b128 v[186:189], v222 offset:38912
	ds_read_b128 v[212:215], v222 offset:39936
	buffer_load_dwordx4 v1, s[40:43], s87 offen lds
	s_mov_b32 m0, s75
	s_nop 0
	buffer_load_dwordx4 v216, s[40:43], s87 offen lds
	s_waitcnt vmcnt(8)
	s_waitcnt lgkmcnt(0)
	s_barrier
	s_waitcnt lgkmcnt(7)
	v_mfma_f32_16x16x32_bf16 v[126:129], v[130:133], v[162:165], v[126:129]
	v_mfma_f32_16x16x32_bf16 v[126:129], v[134:137], v[166:169], v[126:129]
	s_waitcnt lgkmcnt(5)
	v_mfma_f32_16x16x32_bf16 v[122:125], v[138:141], v[162:165], v[122:125]
	v_mfma_f32_16x16x32_bf16 v[122:125], v[142:145], v[166:169], v[122:125]
	s_waitcnt lgkmcnt(3)
	v_mfma_f32_16x16x32_bf16 v[114:117], v[130:133], v[170:173], v[114:117]
	v_mfma_f32_16x16x32_bf16 v[114:117], v[134:137], v[174:177], v[114:117]
	s_waitcnt lgkmcnt(1)
	v_mfma_f32_16x16x32_bf16 v[106:109], v[138:141], v[170:173], v[106:109]
	v_mfma_f32_16x16x32_bf16 v[106:109], v[142:145], v[174:177], v[106:109]
	v_mfma_f32_16x16x32_bf16 v[102:105], v[130:133], v[178:181], v[102:105]
	v_mfma_f32_16x16x32_bf16 v[102:105], v[134:137], v[182:185], v[102:105]
	v_mfma_f32_16x16x32_bf16 v[94:97], v[138:141], v[178:181], v[94:97]
	v_mfma_f32_16x16x32_bf16 v[94:97], v[142:145], v[182:185], v[94:97]
	v_mfma_f32_16x16x32_bf16 v[86:89], v[130:133], v[186:189], v[86:89]
	v_mfma_f32_16x16x32_bf16 v[86:89], v[134:137], v[212:215], v[86:89]
	s_waitcnt lgkmcnt(0)
	v_mfma_f32_16x16x32_bf16 v[78:81], v[138:141], v[186:189], v[78:81]
	v_mfma_f32_16x16x32_bf16 v[78:81], v[142:145], v[212:215], v[78:81]
	v_mfma_f32_16x16x32_bf16 v[118:121], v[146:149], v[162:165], v[118:121]
	v_mfma_f32_16x16x32_bf16 v[118:121], v[150:153], v[166:169], v[118:121]
	v_mfma_f32_16x16x32_bf16 v[110:113], v[154:157], v[162:165], v[110:113]
	v_mfma_f32_16x16x32_bf16 v[110:113], v[158:161], v[166:169], v[110:113]
	v_mfma_f32_16x16x32_bf16 v[98:101], v[146:149], v[170:173], v[98:101]
	v_mfma_f32_16x16x32_bf16 v[98:101], v[150:153], v[174:177], v[98:101]
	v_mfma_f32_16x16x32_bf16 v[90:93], v[154:157], v[170:173], v[90:93]
	v_mfma_f32_16x16x32_bf16 v[90:93], v[158:161], v[174:177], v[90:93]
	v_mfma_f32_16x16x32_bf16 v[82:85], v[146:149], v[178:181], v[82:85]
	v_mfma_f32_16x16x32_bf16 v[82:85], v[150:153], v[182:185], v[82:85]
	v_mfma_f32_16x16x32_bf16 v[74:77], v[154:157], v[178:181], v[74:77]
	v_mfma_f32_16x16x32_bf16 v[74:77], v[158:161], v[182:185], v[74:77]
	v_mfma_f32_16x16x32_bf16 v[70:73], v[146:149], v[186:189], v[70:73]
	v_mfma_f32_16x16x32_bf16 v[70:73], v[150:153], v[212:215], v[70:73]
	v_mfma_f32_16x16x32_bf16 v[66:69], v[154:157], v[186:189], v[66:69]
	v_mfma_f32_16x16x32_bf16 v[66:69], v[158:161], v[212:215], v[66:69]
	s_barrier
	s_mov_b32 m0, s79
	s_or_b32 s87, s86, 0x80
	ds_read_b128 v[162:165], v222 offset:49152
	ds_read_b128 v[166:169], v222 offset:50176
	ds_read_b128 v[170:173], v222 offset:51200
	ds_read_b128 v[174:177], v222 offset:52224
	ds_read_b128 v[178:181], v222 offset:53248
	ds_read_b128 v[182:185], v222 offset:54272
	ds_read_b128 v[186:189], v222 offset:55296
	ds_read_b128 v[212:215], v222 offset:56320
	buffer_load_dwordx4 v191, s[44:47], s87 offen lds
	s_mov_b32 m0, s80
	s_add_i32 s86, s86, 0x80080
	buffer_load_dwordx4 v217, s[44:47], s87 offen lds
	s_mov_b32 m0, s83
	s_nop 0
	buffer_load_dwordx4 v191, s[44:47], s86 offen lds
	s_mov_b32 m0, s92
	s_nop 0
	buffer_load_dwordx4 v217, s[44:47], s86 offen lds
	s_mov_b32 m0, s81
	s_nop 0
	buffer_load_dwordx4 v1, s[40:43], s85 offen lds
	s_mov_b32 m0, s82
	s_nop 0
	buffer_load_dwordx4 v216, s[40:43], s85 offen lds
	s_waitcnt vmcnt(8)
	s_waitcnt lgkmcnt(0)
	s_barrier
	s_waitcnt lgkmcnt(7)
	v_mfma_f32_16x16x32_bf16 v[62:65], v[130:133], v[162:165], v[62:65]
	v_mfma_f32_16x16x32_bf16 v[62:65], v[134:137], v[166:169], v[62:65]
	s_waitcnt lgkmcnt(5)
	v_mfma_f32_16x16x32_bf16 v[58:61], v[138:141], v[162:165], v[58:61]
	v_mfma_f32_16x16x32_bf16 v[58:61], v[142:145], v[166:169], v[58:61]
	s_waitcnt lgkmcnt(3)
	v_mfma_f32_16x16x32_bf16 v[54:57], v[130:133], v[170:173], v[54:57]
	v_mfma_f32_16x16x32_bf16 v[54:57], v[134:137], v[174:177], v[54:57]
	s_waitcnt lgkmcnt(1)
	v_mfma_f32_16x16x32_bf16 v[46:49], v[138:141], v[170:173], v[46:49]
	v_mfma_f32_16x16x32_bf16 v[46:49], v[142:145], v[174:177], v[46:49]
	v_mfma_f32_16x16x32_bf16 v[38:41], v[130:133], v[178:181], v[38:41]
	v_mfma_f32_16x16x32_bf16 v[38:41], v[134:137], v[182:185], v[38:41]
	v_mfma_f32_16x16x32_bf16 v[30:33], v[138:141], v[178:181], v[30:33]
	v_mfma_f32_16x16x32_bf16 v[30:33], v[142:145], v[182:185], v[30:33]
	v_mfma_f32_16x16x32_bf16 v[22:25], v[130:133], v[186:189], v[22:25]
	v_mfma_f32_16x16x32_bf16 v[22:25], v[134:137], v[212:215], v[22:25]
	s_waitcnt lgkmcnt(0)
	v_mfma_f32_16x16x32_bf16 v[14:17], v[138:141], v[186:189], v[14:17]
	v_mfma_f32_16x16x32_bf16 v[14:17], v[142:145], v[212:215], v[14:17]
	v_mfma_f32_16x16x32_bf16 v[50:53], v[146:149], v[162:165], v[50:53]
	v_mfma_f32_16x16x32_bf16 v[50:53], v[150:153], v[166:169], v[50:53]
	v_mfma_f32_16x16x32_bf16 v[42:45], v[154:157], v[162:165], v[42:45]
	v_mfma_f32_16x16x32_bf16 v[42:45], v[158:161], v[166:169], v[42:45]
	v_mfma_f32_16x16x32_bf16 v[34:37], v[146:149], v[170:173], v[34:37]
	v_mfma_f32_16x16x32_bf16 v[34:37], v[150:153], v[174:177], v[34:37]
	v_mfma_f32_16x16x32_bf16 v[26:29], v[154:157], v[170:173], v[26:29]
	v_mfma_f32_16x16x32_bf16 v[26:29], v[158:161], v[174:177], v[26:29]
	v_mfma_f32_16x16x32_bf16 v[18:21], v[146:149], v[178:181], v[18:21]
	v_mfma_f32_16x16x32_bf16 v[18:21], v[150:153], v[182:185], v[18:21]
	v_mfma_f32_16x16x32_bf16 v[10:13], v[154:157], v[178:181], v[10:13]
	v_mfma_f32_16x16x32_bf16 v[10:13], v[158:161], v[182:185], v[10:13]
	v_mfma_f32_16x16x32_bf16 v[6:9], v[146:149], v[186:189], v[6:9]
	v_mfma_f32_16x16x32_bf16 v[6:9], v[150:153], v[212:215], v[6:9]
	v_mfma_f32_16x16x32_bf16 v[2:5], v[154:157], v[186:189], v[2:5]
	v_mfma_f32_16x16x32_bf16 v[2:5], v[158:161], v[212:215], v[2:5]
	s_barrier
	s_add_i32 s84, s84, 2
	s_addk_i32 s64, 0x100
	s_addk_i32 s65, 0x100
	s_cmp_gt_u32 s84, 29
	s_cbranch_scc0 .LBB0_114
	s_and_b64 vcc, exec, s[56:57]
	s_cbranch_vccz .LBB0_127
	s_barrier
	s_cmp_gt_i32 s61, 23
	s_mov_b64 s[46:47], -1
	s_cbranch_scc1 .LBB0_128

.LBB0_686:
	v_add_u32_e32 v152, 0x10000, v138
	v_add_u32_e32 v168, 0x14000, v138
	ds_read_b128 v[140:143], v152
	ds_read_b128 v[144:147], v152 offset:1024
	ds_read_b128 v[148:151], v152 offset:2048
	ds_read_b128 v[152:155], v152 offset:3072
	ds_read_b128 v[156:159], v168
	ds_read_b128 v[160:163], v168 offset:1024
	ds_read_b128 v[164:167], v168 offset:2048
	ds_read_b128 v[168:171], v168 offset:3072
	s_add_i32 s10, s33, s52
	s_add_i32 s53, s27, s52
	s_add_i32 s11, s10, 0x1000
	s_addk_i32 s53, 0x1000
	s_cmp_eq_u32 s52, 0
	s_cselect_b32 s55, s49, s11
	s_cselect_b32 s54, s50, s53
	s_or_b32 s53, s55, 0x80
	s_add_i32 s10, s10, 0x80f80
	s_mov_b32 m0, s43
	ds_read_b128 v[172:175], v139
	ds_read_b128 v[176:179], v139 offset:1024
	ds_read_b128 v[180:183], v139 offset:2048
	ds_read_b128 v[184:187], v139 offset:3072
	ds_read_b128 v[188:191], v139 offset:4096
	ds_read_b128 v[192:195], v139 offset:5120
	ds_read_b128 v[196:199], v139 offset:6144
	ds_read_b128 v[200:203], v139 offset:7168
	buffer_load_dwordx4 v134, s[4:7], s10 offen lds
	s_mov_b32 m0, s44
	s_nop 0
	buffer_load_dwordx4 v136, s[4:7], s10 offen lds
	s_waitcnt vmcnt(8)
	s_waitcnt lgkmcnt(0)
	s_barrier
	s_waitcnt lgkmcnt(7)
	v_mfma_f32_16x16x32_bf16 v[126:129], v[140:143], v[172:175], v[126:129]
	v_mfma_f32_16x16x32_bf16 v[126:129], v[144:147], v[176:179], v[126:129]
	s_waitcnt lgkmcnt(5)
	v_mfma_f32_16x16x32_bf16 v[122:125], v[148:151], v[172:175], v[122:125]
	v_mfma_f32_16x16x32_bf16 v[122:125], v[152:155], v[176:179], v[122:125]
	s_waitcnt lgkmcnt(3)
	v_mfma_f32_16x16x32_bf16 v[110:113], v[140:143], v[180:183], v[110:113]
	v_mfma_f32_16x16x32_bf16 v[110:113], v[144:147], v[184:187], v[110:113]
	s_waitcnt lgkmcnt(1)
	v_mfma_f32_16x16x32_bf16 v[106:109], v[148:151], v[180:183], v[106:109]
	v_mfma_f32_16x16x32_bf16 v[106:109], v[152:155], v[184:187], v[106:109]
	v_mfma_f32_16x16x32_bf16 v[98:101], v[140:143], v[188:191], v[98:101]
	v_mfma_f32_16x16x32_bf16 v[98:101], v[144:147], v[192:195], v[98:101]
	v_mfma_f32_16x16x32_bf16 v[90:93], v[148:151], v[188:191], v[90:93]
	v_mfma_f32_16x16x32_bf16 v[90:93], v[152:155], v[192:195], v[90:93]
	v_mfma_f32_16x16x32_bf16 v[82:85], v[140:143], v[196:199], v[82:85]
	v_mfma_f32_16x16x32_bf16 v[82:85], v[144:147], v[200:203], v[82:85]
	s_waitcnt lgkmcnt(0)
	v_mfma_f32_16x16x32_bf16 v[74:77], v[148:151], v[196:199], v[74:77]
	v_mfma_f32_16x16x32_bf16 v[74:77], v[152:155], v[200:203], v[74:77]
	v_mfma_f32_16x16x32_bf16 v[118:121], v[156:159], v[172:175], v[118:121]
	v_mfma_f32_16x16x32_bf16 v[118:121], v[160:163], v[176:179], v[118:121]
	v_mfma_f32_16x16x32_bf16 v[114:117], v[164:167], v[172:175], v[114:117]
	v_mfma_f32_16x16x32_bf16 v[114:117], v[168:171], v[176:179], v[114:117]
	v_mfma_f32_16x16x32_bf16 v[102:105], v[156:159], v[180:183], v[102:105]
	v_mfma_f32_16x16x32_bf16 v[102:105], v[160:163], v[184:187], v[102:105]
	v_mfma_f32_16x16x32_bf16 v[94:97], v[164:167], v[180:183], v[94:97]
	v_mfma_f32_16x16x32_bf16 v[94:97], v[168:171], v[184:187], v[94:97]
	v_mfma_f32_16x16x32_bf16 v[86:89], v[156:159], v[188:191], v[86:89]
	v_mfma_f32_16x16x32_bf16 v[86:89], v[160:163], v[192:195], v[86:89]
	v_mfma_f32_16x16x32_bf16 v[78:81], v[164:167], v[188:191], v[78:81]
	v_mfma_f32_16x16x32_bf16 v[78:81], v[168:171], v[192:195], v[78:81]
	v_mfma_f32_16x16x32_bf16 v[70:73], v[156:159], v[196:199], v[70:73]
	v_mfma_f32_16x16x32_bf16 v[70:73], v[160:163], v[200:203], v[70:73]
	v_mfma_f32_16x16x32_bf16 v[66:69], v[164:167], v[196:199], v[66:69]
	v_mfma_f32_16x16x32_bf16 v[66:69], v[168:171], v[200:203], v[66:69]
	s_barrier
	s_mov_b32 m0, s26
	s_mov_b32 s10, s6
	s_mov_b32 s11, s7
	ds_read_b128 v[172:175], v139 offset:16384
	ds_read_b128 v[176:179], v139 offset:17408
	ds_read_b128 v[180:183], v139 offset:18432
	ds_read_b128 v[184:187], v139 offset:19456
	ds_read_b128 v[188:191], v139 offset:20480
	ds_read_b128 v[192:195], v139 offset:21504
	ds_read_b128 v[196:199], v139 offset:22528
	ds_read_b128 v[200:203], v139 offset:23552
	buffer_load_dwordx4 v135, s[8:11], s54 offen lds
	s_mov_b32 m0, s28
	s_add_i32 s56, s54, 0x80000
	buffer_load_dwordx4 v137, s[8:11], s54 offen lds
	s_mov_b32 m0, s29
	s_nop 0
	buffer_load_dwordx4 v135, s[8:11], s56 offen lds
	s_mov_b32 m0, s30
	s_nop 0
	buffer_load_dwordx4 v137, s[8:11], s56 offen lds
	s_mov_b32 m0, s25
	s_nop 0
	buffer_load_dwordx4 v134, s[4:7], s55 offen lds
	s_mov_b32 m0, s31
	s_nop 0
	buffer_load_dwordx4 v136, s[4:7], s55 offen lds
	s_waitcnt vmcnt(8)
	s_waitcnt lgkmcnt(0)
	s_barrier
	s_waitcnt lgkmcnt(7)
	v_mfma_f32_16x16x32_bf16 v[62:65], v[140:143], v[172:175], v[62:65]
	v_mfma_f32_16x16x32_bf16 v[62:65], v[144:147], v[176:179], v[62:65]
	s_waitcnt lgkmcnt(5)
	v_mfma_f32_16x16x32_bf16 v[58:61], v[148:151], v[172:175], v[58:61]
	v_mfma_f32_16x16x32_bf16 v[58:61], v[152:155], v[176:179], v[58:61]
	s_waitcnt lgkmcnt(3)
	v_mfma_f32_16x16x32_bf16 v[46:49], v[140:143], v[180:183], v[46:49]
	v_mfma_f32_16x16x32_bf16 v[46:49], v[144:147], v[184:187], v[46:49]
	s_waitcnt lgkmcnt(1)
	v_mfma_f32_16x16x32_bf16 v[42:45], v[148:151], v[180:183], v[42:45]
	v_mfma_f32_16x16x32_bf16 v[42:45], v[152:155], v[184:187], v[42:45]
	v_mfma_f32_16x16x32_bf16 v[30:33], v[140:143], v[188:191], v[30:33]
	v_mfma_f32_16x16x32_bf16 v[30:33], v[144:147], v[192:195], v[30:33]
	v_mfma_f32_16x16x32_bf16 v[26:29], v[148:151], v[188:191], v[26:29]
	v_mfma_f32_16x16x32_bf16 v[26:29], v[152:155], v[192:195], v[26:29]
	v_mfma_f32_16x16x32_bf16 v[14:17], v[140:143], v[196:199], v[14:17]
	v_mfma_f32_16x16x32_bf16 v[14:17], v[144:147], v[200:203], v[14:17]
	s_waitcnt lgkmcnt(0)
	v_mfma_f32_16x16x32_bf16 v[10:13], v[148:151], v[196:199], v[10:13]
	v_mfma_f32_16x16x32_bf16 v[10:13], v[152:155], v[200:203], v[10:13]
	v_mfma_f32_16x16x32_bf16 v[54:57], v[156:159], v[172:175], v[54:57]
	v_mfma_f32_16x16x32_bf16 v[54:57], v[160:163], v[176:179], v[54:57]
	v_mfma_f32_16x16x32_bf16 v[50:53], v[164:167], v[172:175], v[50:53]
	v_mfma_f32_16x16x32_bf16 v[50:53], v[168:171], v[176:179], v[50:53]
	v_mfma_f32_16x16x32_bf16 v[38:41], v[156:159], v[180:183], v[38:41]
	v_mfma_f32_16x16x32_bf16 v[38:41], v[160:163], v[184:187], v[38:41]
	v_mfma_f32_16x16x32_bf16 v[34:37], v[164:167], v[180:183], v[34:37]
	v_mfma_f32_16x16x32_bf16 v[34:37], v[168:171], v[184:187], v[34:37]
	v_mfma_f32_16x16x32_bf16 v[22:25], v[156:159], v[188:191], v[22:25]
	v_mfma_f32_16x16x32_bf16 v[22:25], v[160:163], v[192:195], v[22:25]
	v_mfma_f32_16x16x32_bf16 v[18:21], v[164:167], v[188:191], v[18:21]
	v_mfma_f32_16x16x32_bf16 v[18:21], v[168:171], v[192:195], v[18:21]
	v_mfma_f32_16x16x32_bf16 v[6:9], v[156:159], v[196:199], v[6:9]
	v_mfma_f32_16x16x32_bf16 v[6:9], v[160:163], v[200:203], v[6:9]
	v_mfma_f32_16x16x32_bf16 v[2:5], v[164:167], v[196:199], v[2:5]
	v_mfma_f32_16x16x32_bf16 v[2:5], v[168:171], v[200:203], v[2:5]
	s_barrier
	v_add_u32_e32 v152, 0x18000, v138
	v_add_u32_e32 v168, 0x1c000, v138
	ds_read_b128 v[140:143], v152
	ds_read_b128 v[144:147], v152 offset:1024
	ds_read_b128 v[148:151], v152 offset:2048
	ds_read_b128 v[152:155], v152 offset:3072
	ds_read_b128 v[156:159], v168
	ds_read_b128 v[160:163], v168 offset:1024
	ds_read_b128 v[164:167], v168 offset:2048
	ds_read_b128 v[168:171], v168 offset:3072
	s_add_i32 s55, s55, 0x80000
	s_mov_b32 m0, s34
	ds_read_b128 v[172:175], v139 offset:32768
	ds_read_b128 v[176:179], v139 offset:33792
	ds_read_b128 v[180:183], v139 offset:34816
	ds_read_b128 v[184:187], v139 offset:35840
	ds_read_b128 v[188:191], v139 offset:36864
	ds_read_b128 v[192:195], v139 offset:37888
	ds_read_b128 v[196:199], v139 offset:38912
	ds_read_b128 v[200:203], v139 offset:39936
	buffer_load_dwordx4 v134, s[4:7], s55 offen lds
	s_mov_b32 m0, s35
	s_nop 0
	buffer_load_dwordx4 v136, s[4:7], s55 offen lds
	s_waitcnt vmcnt(8)
	s_waitcnt lgkmcnt(0)
	s_barrier
	s_waitcnt lgkmcnt(7)
	v_mfma_f32_16x16x32_bf16 v[126:129], v[140:143], v[172:175], v[126:129]
	v_mfma_f32_16x16x32_bf16 v[126:129], v[144:147], v[176:179], v[126:129]
	s_waitcnt lgkmcnt(5)
	v_mfma_f32_16x16x32_bf16 v[122:125], v[148:151], v[172:175], v[122:125]
	v_mfma_f32_16x16x32_bf16 v[122:125], v[152:155], v[176:179], v[122:125]
	s_waitcnt lgkmcnt(3)
	v_mfma_f32_16x16x32_bf16 v[110:113], v[140:143], v[180:183], v[110:113]
	v_mfma_f32_16x16x32_bf16 v[110:113], v[144:147], v[184:187], v[110:113]
	s_waitcnt lgkmcnt(1)
	v_mfma_f32_16x16x32_bf16 v[106:109], v[148:151], v[180:183], v[106:109]
	v_mfma_f32_16x16x32_bf16 v[106:109], v[152:155], v[184:187], v[106:109]
	v_mfma_f32_16x16x32_bf16 v[98:101], v[140:143], v[188:191], v[98:101]
	v_mfma_f32_16x16x32_bf16 v[98:101], v[144:147], v[192:195], v[98:101]
	v_mfma_f32_16x16x32_bf16 v[90:93], v[148:151], v[188:191], v[90:93]
	v_mfma_f32_16x16x32_bf16 v[90:93], v[152:155], v[192:195], v[90:93]
	v_mfma_f32_16x16x32_bf16 v[82:85], v[140:143], v[196:199], v[82:85]
	v_mfma_f32_16x16x32_bf16 v[82:85], v[144:147], v[200:203], v[82:85]
	s_waitcnt lgkmcnt(0)
	v_mfma_f32_16x16x32_bf16 v[74:77], v[148:151], v[196:199], v[74:77]
	v_mfma_f32_16x16x32_bf16 v[74:77], v[152:155], v[200:203], v[74:77]
	v_mfma_f32_16x16x32_bf16 v[118:121], v[156:159], v[172:175], v[118:121]
	v_mfma_f32_16x16x32_bf16 v[118:121], v[160:163], v[176:179], v[118:121]
	v_mfma_f32_16x16x32_bf16 v[114:117], v[164:167], v[172:175], v[114:117]
	v_mfma_f32_16x16x32_bf16 v[114:117], v[168:171], v[176:179], v[114:117]
	v_mfma_f32_16x16x32_bf16 v[102:105], v[156:159], v[180:183], v[102:105]
	v_mfma_f32_16x16x32_bf16 v[102:105], v[160:163], v[184:187], v[102:105]
	v_mfma_f32_16x16x32_bf16 v[94:97], v[164:167], v[180:183], v[94:97]
	v_mfma_f32_16x16x32_bf16 v[94:97], v[168:171], v[184:187], v[94:97]
	v_mfma_f32_16x16x32_bf16 v[86:89], v[156:159], v[188:191], v[86:89]
	v_mfma_f32_16x16x32_bf16 v[86:89], v[160:163], v[192:195], v[86:89]
	v_mfma_f32_16x16x32_bf16 v[78:81], v[164:167], v[188:191], v[78:81]
	v_mfma_f32_16x16x32_bf16 v[78:81], v[168:171], v[192:195], v[78:81]
	v_mfma_f32_16x16x32_bf16 v[70:73], v[156:159], v[196:199], v[70:73]
	v_mfma_f32_16x16x32_bf16 v[70:73], v[160:163], v[200:203], v[70:73]
	v_mfma_f32_16x16x32_bf16 v[66:69], v[164:167], v[196:199], v[66:69]
	v_mfma_f32_16x16x32_bf16 v[66:69], v[168:171], v[200:203], v[66:69]
	s_barrier
	s_mov_b32 m0, s36
	s_or_b32 s55, s54, 0x80
	ds_read_b128 v[172:175], v139 offset:49152
	ds_read_b128 v[176:179], v139 offset:50176
	ds_read_b128 v[180:183], v139 offset:51200
	ds_read_b128 v[184:187], v139 offset:52224
	ds_read_b128 v[188:191], v139 offset:53248
	ds_read_b128 v[192:195], v139 offset:54272
	ds_read_b128 v[196:199], v139 offset:55296
	ds_read_b128 v[200:203], v139 offset:56320
	buffer_load_dwordx4 v135, s[8:11], s55 offen lds
	s_mov_b32 m0, s37
	s_add_i32 s54, s54, 0x80080
	buffer_load_dwordx4 v137, s[8:11], s55 offen lds
	s_mov_b32 m0, s41
	s_nop 0
	buffer_load_dwordx4 v135, s[8:11], s54 offen lds
	s_mov_b32 m0, s42
	s_nop 0
	buffer_load_dwordx4 v137, s[8:11], s54 offen lds
	s_mov_b32 m0, s38
	s_nop 0
	buffer_load_dwordx4 v134, s[4:7], s53 offen lds
	s_mov_b32 m0, s40
	s_nop 0
	buffer_load_dwordx4 v136, s[4:7], s53 offen lds
	s_waitcnt vmcnt(8)
	s_waitcnt lgkmcnt(0)
	s_barrier
	s_waitcnt lgkmcnt(7)
	v_mfma_f32_16x16x32_bf16 v[62:65], v[140:143], v[172:175], v[62:65]
	v_mfma_f32_16x16x32_bf16 v[62:65], v[144:147], v[176:179], v[62:65]
	s_waitcnt lgkmcnt(5)
	v_mfma_f32_16x16x32_bf16 v[58:61], v[148:151], v[172:175], v[58:61]
	v_mfma_f32_16x16x32_bf16 v[58:61], v[152:155], v[176:179], v[58:61]
	s_waitcnt lgkmcnt(3)
	v_mfma_f32_16x16x32_bf16 v[46:49], v[140:143], v[180:183], v[46:49]
	v_mfma_f32_16x16x32_bf16 v[46:49], v[144:147], v[184:187], v[46:49]
	s_waitcnt lgkmcnt(1)
	v_mfma_f32_16x16x32_bf16 v[42:45], v[148:151], v[180:183], v[42:45]
	v_mfma_f32_16x16x32_bf16 v[42:45], v[152:155], v[184:187], v[42:45]
	v_mfma_f32_16x16x32_bf16 v[30:33], v[140:143], v[188:191], v[30:33]
	v_mfma_f32_16x16x32_bf16 v[30:33], v[144:147], v[192:195], v[30:33]
	v_mfma_f32_16x16x32_bf16 v[26:29], v[148:151], v[188:191], v[26:29]
	v_mfma_f32_16x16x32_bf16 v[26:29], v[152:155], v[192:195], v[26:29]
	v_mfma_f32_16x16x32_bf16 v[14:17], v[140:143], v[196:199], v[14:17]
	v_mfma_f32_16x16x32_bf16 v[14:17], v[144:147], v[200:203], v[14:17]
	s_waitcnt lgkmcnt(0)
	v_mfma_f32_16x16x32_bf16 v[10:13], v[148:151], v[196:199], v[10:13]
	v_mfma_f32_16x16x32_bf16 v[10:13], v[152:155], v[200:203], v[10:13]
	v_mfma_f32_16x16x32_bf16 v[54:57], v[156:159], v[172:175], v[54:57]
	v_mfma_f32_16x16x32_bf16 v[54:57], v[160:163], v[176:179], v[54:57]
	v_mfma_f32_16x16x32_bf16 v[50:53], v[164:167], v[172:175], v[50:53]
	v_mfma_f32_16x16x32_bf16 v[50:53], v[168:171], v[176:179], v[50:53]
	v_mfma_f32_16x16x32_bf16 v[38:41], v[156:159], v[180:183], v[38:41]
	v_mfma_f32_16x16x32_bf16 v[38:41], v[160:163], v[184:187], v[38:41]
	v_mfma_f32_16x16x32_bf16 v[34:37], v[164:167], v[180:183], v[34:37]
	v_mfma_f32_16x16x32_bf16 v[34:37], v[168:171], v[184:187], v[34:37]
	v_mfma_f32_16x16x32_bf16 v[22:25], v[156:159], v[188:191], v[22:25]
	v_mfma_f32_16x16x32_bf16 v[22:25], v[160:163], v[192:195], v[22:25]
	v_mfma_f32_16x16x32_bf16 v[18:21], v[164:167], v[188:191], v[18:21]
	v_mfma_f32_16x16x32_bf16 v[18:21], v[168:171], v[192:195], v[18:21]
	v_mfma_f32_16x16x32_bf16 v[6:9], v[156:159], v[196:199], v[6:9]
	v_mfma_f32_16x16x32_bf16 v[6:9], v[160:163], v[200:203], v[6:9]
	v_mfma_f32_16x16x32_bf16 v[2:5], v[164:167], v[196:199], v[2:5]
	v_mfma_f32_16x16x32_bf16 v[2:5], v[168:171], v[200:203], v[2:5]
	s_barrier
	s_add_i32 s51, s51, 2
	s_addk_i32 s52, 0x100
	s_cmp_gt_u32 s51, 29
	s_cbranch_scc0 .LBB0_686
	s_andn2_b64 vcc, exec, s[2:3]
	s_cbranch_vccnz .LBB0_678
	v_mov_b32_e32 v2, 0
	s_mov_b32 s14, s46
	s_mov_b32 s15, s47
	s_mov_b32 s27, s48
	s_mov_b32 s33, s13
	s_mov_b32 s45, s12
	v_mov_b32_e32 v3, v2
	v_mov_b32_e32 v4, v2
	v_mov_b32_e32 v5, v2
	v_mov_b32_e32 v6, v2
	v_mov_b32_e32 v7, v2
	v_mov_b32_e32 v8, v2
	v_mov_b32_e32 v9, v2
	v_mov_b32_e32 v18, v2
	v_mov_b32_e32 v19, v2
	v_mov_b32_e32 v20, v2
	v_mov_b32_e32 v21, v2
	v_mov_b32_e32 v22, v2
	v_mov_b32_e32 v23, v2
	v_mov_b32_e32 v24, v2
	v_mov_b32_e32 v25, v2
	v_mov_b32_e32 v34, v2
	v_mov_b32_e32 v35, v2
	v_mov_b32_e32 v36, v2
	v_mov_b32_e32 v37, v2
	v_mov_b32_e32 v38, v2
	v_mov_b32_e32 v39, v2
	v_mov_b32_e32 v40, v2
	v_mov_b32_e32 v41, v2
	v_mov_b32_e32 v50, v2
	v_mov_b32_e32 v51, v2
	v_mov_b32_e32 v52, v2
	v_mov_b32_e32 v53, v2
	v_mov_b32_e32 v54, v2
	v_mov_b32_e32 v55, v2
	v_mov_b32_e32 v56, v2
	v_mov_b32_e32 v57, v2
	v_mov_b32_e32 v10, v2
	v_mov_b32_e32 v11, v2
	v_mov_b32_e32 v12, v2
	v_mov_b32_e32 v13, v2
	v_mov_b32_e32 v14, v2
	v_mov_b32_e32 v15, v2
	v_mov_b32_e32 v16, v2
	v_mov_b32_e32 v17, v2
	v_mov_b32_e32 v26, v2
	v_mov_b32_e32 v27, v2
	v_mov_b32_e32 v28, v2
	v_mov_b32_e32 v29, v2
	v_mov_b32_e32 v30, v2
	v_mov_b32_e32 v31, v2
	v_mov_b32_e32 v32, v2
	v_mov_b32_e32 v33, v2
	v_mov_b32_e32 v42, v2
	v_mov_b32_e32 v43, v2
	v_mov_b32_e32 v44, v2
	v_mov_b32_e32 v45, v2
	v_mov_b32_e32 v46, v2
	v_mov_b32_e32 v47, v2
	v_mov_b32_e32 v48, v2
	v_mov_b32_e32 v49, v2
	v_mov_b32_e32 v58, v2
	v_mov_b32_e32 v59, v2
	v_mov_b32_e32 v60, v2
	v_mov_b32_e32 v61, v2
	v_mov_b32_e32 v62, v2
	v_mov_b32_e32 v63, v2
	v_mov_b32_e32 v64, v2
	v_mov_b32_e32 v65, v2
	v_mov_b32_e32 v66, v2
	v_mov_b32_e32 v67, v2
	v_mov_b32_e32 v68, v2
	v_mov_b32_e32 v69, v2
	v_mov_b32_e32 v70, v2
	v_mov_b32_e32 v71, v2
	v_mov_b32_e32 v72, v2
	v_mov_b32_e32 v73, v2
	v_mov_b32_e32 v78, v2
	v_mov_b32_e32 v79, v2
	v_mov_b32_e32 v80, v2
	v_mov_b32_e32 v81, v2
	v_mov_b32_e32 v86, v2
	v_mov_b32_e32 v87, v2
	v_mov_b32_e32 v88, v2
	v_mov_b32_e32 v89, v2
	v_mov_b32_e32 v94, v2
	v_mov_b32_e32 v95, v2
	v_mov_b32_e32 v96, v2
	v_mov_b32_e32 v97, v2
	v_mov_b32_e32 v102, v2
	v_mov_b32_e32 v103, v2
	v_mov_b32_e32 v104, v2
	v_mov_b32_e32 v105, v2
	v_mov_b32_e32 v114, v2
	v_mov_b32_e32 v115, v2
	v_mov_b32_e32 v116, v2
	v_mov_b32_e32 v117, v2
	v_mov_b32_e32 v118, v2
	v_mov_b32_e32 v119, v2
	v_mov_b32_e32 v120, v2
	v_mov_b32_e32 v121, v2
	v_mov_b32_e32 v74, v2
	v_mov_b32_e32 v75, v2
	v_mov_b32_e32 v76, v2
	v_mov_b32_e32 v77, v2
	v_mov_b32_e32 v82, v2
	v_mov_b32_e32 v83, v2
	v_mov_b32_e32 v84, v2
	v_mov_b32_e32 v85, v2
	v_mov_b32_e32 v90, v2
	v_mov_b32_e32 v91, v2
	v_mov_b32_e32 v92, v2
	v_mov_b32_e32 v93, v2
	v_mov_b32_e32 v98, v2
	v_mov_b32_e32 v99, v2
	v_mov_b32_e32 v100, v2
	v_mov_b32_e32 v101, v2
	v_mov_b32_e32 v106, v2
	v_mov_b32_e32 v107, v2
	v_mov_b32_e32 v108, v2
	v_mov_b32_e32 v109, v2
	v_mov_b32_e32 v110, v2
	v_mov_b32_e32 v111, v2
	v_mov_b32_e32 v112, v2
	v_mov_b32_e32 v113, v2
	v_mov_b32_e32 v122, v2
	v_mov_b32_e32 v123, v2
	v_mov_b32_e32 v124, v2
	v_mov_b32_e32 v125, v2
	v_mov_b32_e32 v126, v2
	v_mov_b32_e32 v127, v2
	v_mov_b32_e32 v128, v2
	v_mov_b32_e32 v129, v2
	s_branch .LBB0_678

.LBB0_907:
	v_add_u32_e32 v166, 0x10000, v179
	ds_read_b128 v[162:165], v166
	ds_read_b128 v[182:185], v166 offset:1024
	ds_read_b128 v[186:189], v166 offset:2048
	ds_read_b128 v[190:193], v166 offset:3072
	v_add_u32_e32 v166, 0x14000, v179
	ds_read_b128 v[194:197], v166
	ds_read_b128 v[198:201], v166 offset:1024
	ds_read_b128 v[202:205], v166 offset:2048
	ds_read_b128 v[206:209], v166 offset:3072
	s_add_i32 s10, s45, s64
	s_add_i32 s26, s40, s64
	s_add_i32 s11, s10, 0x1000
	s_addk_i32 s26, 0x1000
	s_cmp_eq_u32 s64, 0
	s_cselect_b32 s29, s62, s11
	s_cselect_b32 s27, s63, s26
	s_add_i32 s26, s29, 0x80
	s_add_i32 s28, s27, 0x80
	s_add_i32 s10, s10, 0x80f80
	s_mov_b32 m0, s55
	ds_read_b128 v[210:213], v180
	ds_read_b128 v[214:217], v180 offset:1024
	ds_read_b128 v[218:221], v180 offset:2048
	ds_read_b128 v[222:225], v180 offset:3072
	ds_read_b128 v[226:229], v180 offset:4096
	ds_read_b128 v[230:233], v180 offset:5120
	ds_read_b128 v[234:237], v180 offset:6144
	ds_read_b128 v[238:241], v180 offset:7168
	buffer_load_dwordx4 v1, s[4:7], s10 offen lds
	s_mov_b32 m0, s56
	s_nop 0
	buffer_load_dwordx4 v175, s[4:7], s10 offen lds
	s_waitcnt vmcnt(8)
	s_waitcnt lgkmcnt(0)
	s_barrier
	s_waitcnt lgkmcnt(7)
	v_mfma_f32_16x16x32_bf16 v[126:129], v[162:165], v[210:213], v[126:129]
	v_mfma_f32_16x16x32_bf16 v[126:129], v[182:185], v[214:217], v[126:129]
	s_waitcnt lgkmcnt(5)
	v_mfma_f32_16x16x32_bf16 v[122:125], v[186:189], v[210:213], v[122:125]
	v_mfma_f32_16x16x32_bf16 v[122:125], v[190:193], v[214:217], v[122:125]
	s_waitcnt lgkmcnt(3)
	v_mfma_f32_16x16x32_bf16 v[118:121], v[162:165], v[218:221], v[118:121]
	v_mfma_f32_16x16x32_bf16 v[118:121], v[182:185], v[222:225], v[118:121]
	s_waitcnt lgkmcnt(1)
	v_mfma_f32_16x16x32_bf16 v[114:117], v[186:189], v[218:221], v[114:117]
	v_mfma_f32_16x16x32_bf16 v[114:117], v[190:193], v[222:225], v[114:117]
	v_mfma_f32_16x16x32_bf16 v[110:113], v[162:165], v[226:229], v[110:113]
	v_mfma_f32_16x16x32_bf16 v[110:113], v[182:185], v[230:233], v[110:113]
	v_mfma_f32_16x16x32_bf16 v[106:109], v[186:189], v[226:229], v[106:109]
	v_mfma_f32_16x16x32_bf16 v[106:109], v[190:193], v[230:233], v[106:109]
	v_mfma_f32_16x16x32_bf16 v[102:105], v[162:165], v[234:237], v[102:105]
	v_mfma_f32_16x16x32_bf16 v[102:105], v[182:185], v[238:241], v[102:105]
	s_waitcnt lgkmcnt(0)
	v_mfma_f32_16x16x32_bf16 v[98:101], v[186:189], v[234:237], v[98:101]
	v_mfma_f32_16x16x32_bf16 v[98:101], v[190:193], v[238:241], v[98:101]
	v_mfma_f32_16x16x32_bf16 v[94:97], v[194:197], v[210:213], v[94:97]
	v_mfma_f32_16x16x32_bf16 v[94:97], v[198:201], v[214:217], v[94:97]
	v_mfma_f32_16x16x32_bf16 v[90:93], v[202:205], v[210:213], v[90:93]
	v_mfma_f32_16x16x32_bf16 v[90:93], v[206:209], v[214:217], v[90:93]
	v_mfma_f32_16x16x32_bf16 v[86:89], v[194:197], v[218:221], v[86:89]
	v_mfma_f32_16x16x32_bf16 v[86:89], v[198:201], v[222:225], v[86:89]
	v_mfma_f32_16x16x32_bf16 v[82:85], v[202:205], v[218:221], v[82:85]
	v_mfma_f32_16x16x32_bf16 v[82:85], v[206:209], v[222:225], v[82:85]
	v_mfma_f32_16x16x32_bf16 v[78:81], v[194:197], v[226:229], v[78:81]
	v_mfma_f32_16x16x32_bf16 v[78:81], v[198:201], v[230:233], v[78:81]
	v_mfma_f32_16x16x32_bf16 v[74:77], v[202:205], v[226:229], v[74:77]
	v_mfma_f32_16x16x32_bf16 v[74:77], v[206:209], v[230:233], v[74:77]
	v_mfma_f32_16x16x32_bf16 v[70:73], v[194:197], v[234:237], v[70:73]
	v_mfma_f32_16x16x32_bf16 v[70:73], v[198:201], v[238:241], v[70:73]
	v_mfma_f32_16x16x32_bf16 v[66:69], v[202:205], v[234:237], v[66:69]
	v_mfma_f32_16x16x32_bf16 v[66:69], v[206:209], v[238:241], v[66:69]
	s_barrier
	s_mov_b32 m0, s37
	s_mov_b32 s10, s6
	s_mov_b32 s11, s7
	ds_read_b128 v[210:213], v180 offset:16384
	ds_read_b128 v[214:217], v180 offset:17408
	ds_read_b128 v[218:221], v180 offset:18432
	ds_read_b128 v[222:225], v180 offset:19456
	ds_read_b128 v[226:229], v180 offset:20480
	ds_read_b128 v[230:233], v180 offset:21504
	ds_read_b128 v[234:237], v180 offset:22528
	ds_read_b128 v[238:241], v180 offset:23552
	buffer_load_dwordx4 v174, s[8:11], s27 offen lds
	s_mov_b32 m0, s38
	s_add_i32 s66, s27, 0x80000
	buffer_load_dwordx4 v176, s[8:11], s27 offen lds
	s_mov_b32 m0, s39
	s_nop 0
	buffer_load_dwordx4 v174, s[8:11], s66 offen lds
	s_mov_b32 m0, s41
	s_nop 0
	buffer_load_dwordx4 v176, s[8:11], s66 offen lds
	s_mov_b32 m0, s36
	s_nop 0
	buffer_load_dwordx4 v1, s[4:7], s29 offen lds
	s_mov_b32 m0, s42
	s_nop 0
	buffer_load_dwordx4 v175, s[4:7], s29 offen lds
	s_waitcnt vmcnt(8)
	s_waitcnt lgkmcnt(0)
	s_barrier
	s_waitcnt lgkmcnt(7)
	v_mfma_f32_16x16x32_bf16 v[62:65], v[162:165], v[210:213], v[62:65]
	v_mfma_f32_16x16x32_bf16 v[62:65], v[182:185], v[214:217], v[62:65]
	s_waitcnt lgkmcnt(5)
	v_mfma_f32_16x16x32_bf16 v[58:61], v[186:189], v[210:213], v[58:61]
	v_mfma_f32_16x16x32_bf16 v[58:61], v[190:193], v[214:217], v[58:61]
	s_waitcnt lgkmcnt(3)
	v_mfma_f32_16x16x32_bf16 v[54:57], v[162:165], v[218:221], v[54:57]
	v_mfma_f32_16x16x32_bf16 v[54:57], v[182:185], v[222:225], v[54:57]
	s_waitcnt lgkmcnt(1)
	v_mfma_f32_16x16x32_bf16 v[50:53], v[186:189], v[218:221], v[50:53]
	v_mfma_f32_16x16x32_bf16 v[50:53], v[190:193], v[222:225], v[50:53]
	v_mfma_f32_16x16x32_bf16 v[46:49], v[162:165], v[226:229], v[46:49]
	v_mfma_f32_16x16x32_bf16 v[46:49], v[182:185], v[230:233], v[46:49]
	v_mfma_f32_16x16x32_bf16 v[42:45], v[186:189], v[226:229], v[42:45]
	v_mfma_f32_16x16x32_bf16 v[42:45], v[190:193], v[230:233], v[42:45]
	v_mfma_f32_16x16x32_bf16 v[38:41], v[162:165], v[234:237], v[38:41]
	v_mfma_f32_16x16x32_bf16 v[38:41], v[182:185], v[238:241], v[38:41]
	s_waitcnt lgkmcnt(0)
	v_mfma_f32_16x16x32_bf16 v[34:37], v[186:189], v[234:237], v[34:37]
	v_mfma_f32_16x16x32_bf16 v[34:37], v[190:193], v[238:241], v[34:37]
	v_mfma_f32_16x16x32_bf16 v[30:33], v[194:197], v[210:213], v[30:33]
	v_mfma_f32_16x16x32_bf16 v[30:33], v[198:201], v[214:217], v[30:33]
	v_mfma_f32_16x16x32_bf16 v[26:29], v[202:205], v[210:213], v[26:29]
	v_mfma_f32_16x16x32_bf16 v[26:29], v[206:209], v[214:217], v[26:29]
	v_mfma_f32_16x16x32_bf16 v[22:25], v[194:197], v[218:221], v[22:25]
	v_mfma_f32_16x16x32_bf16 v[22:25], v[198:201], v[222:225], v[22:25]
	v_mfma_f32_16x16x32_bf16 v[18:21], v[202:205], v[218:221], v[18:21]
	v_mfma_f32_16x16x32_bf16 v[18:21], v[206:209], v[222:225], v[18:21]
	v_mfma_f32_16x16x32_bf16 v[14:17], v[194:197], v[226:229], v[14:17]
	v_mfma_f32_16x16x32_bf16 v[14:17], v[198:201], v[230:233], v[14:17]
	v_mfma_f32_16x16x32_bf16 v[10:13], v[202:205], v[226:229], v[10:13]
	v_mfma_f32_16x16x32_bf16 v[10:13], v[206:209], v[230:233], v[10:13]
	v_mfma_f32_16x16x32_bf16 v[6:9], v[194:197], v[234:237], v[6:9]
	v_mfma_f32_16x16x32_bf16 v[6:9], v[198:201], v[238:241], v[6:9]
	v_mfma_f32_16x16x32_bf16 v[2:5], v[202:205], v[234:237], v[2:5]
	v_mfma_f32_16x16x32_bf16 v[2:5], v[206:209], v[238:241], v[2:5]
	s_barrier
	v_add_u32_e32 v166, 0x18000, v179
	ds_read_b128 v[162:165], v166
	ds_read_b128 v[182:185], v166 offset:1024
	ds_read_b128 v[186:189], v166 offset:2048
	ds_read_b128 v[190:193], v166 offset:3072
	v_add_u32_e32 v166, 0x1c000, v179
	ds_read_b128 v[194:197], v166
	ds_read_b128 v[198:201], v166 offset:1024
	ds_read_b128 v[202:205], v166 offset:2048
	ds_read_b128 v[206:209], v166 offset:3072
	s_add_i32 s29, s29, 0x80000
	s_mov_b32 m0, s43
	ds_read_b128 v[210:213], v180 offset:32768
	ds_read_b128 v[214:217], v180 offset:33792
	ds_read_b128 v[218:221], v180 offset:34816
	ds_read_b128 v[222:225], v180 offset:35840
	ds_read_b128 v[226:229], v180 offset:36864
	ds_read_b128 v[230:233], v180 offset:37888
	ds_read_b128 v[234:237], v180 offset:38912
	ds_read_b128 v[238:241], v180 offset:39936
	buffer_load_dwordx4 v1, s[4:7], s29 offen lds
	s_mov_b32 m0, s44
	s_nop 0
	buffer_load_dwordx4 v175, s[4:7], s29 offen lds
	s_waitcnt vmcnt(8)
	s_waitcnt lgkmcnt(0)
	s_barrier
	s_waitcnt lgkmcnt(7)
	v_mfma_f32_16x16x32_bf16 v[126:129], v[162:165], v[210:213], v[126:129]
	v_mfma_f32_16x16x32_bf16 v[126:129], v[182:185], v[214:217], v[126:129]
	s_waitcnt lgkmcnt(5)
	v_mfma_f32_16x16x32_bf16 v[122:125], v[186:189], v[210:213], v[122:125]
	v_mfma_f32_16x16x32_bf16 v[122:125], v[190:193], v[214:217], v[122:125]
	s_waitcnt lgkmcnt(3)
	v_mfma_f32_16x16x32_bf16 v[118:121], v[162:165], v[218:221], v[118:121]
	v_mfma_f32_16x16x32_bf16 v[118:121], v[182:185], v[222:225], v[118:121]
	s_waitcnt lgkmcnt(1)
	v_mfma_f32_16x16x32_bf16 v[114:117], v[186:189], v[218:221], v[114:117]
	v_mfma_f32_16x16x32_bf16 v[114:117], v[190:193], v[222:225], v[114:117]
	v_mfma_f32_16x16x32_bf16 v[110:113], v[162:165], v[226:229], v[110:113]
	v_mfma_f32_16x16x32_bf16 v[110:113], v[182:185], v[230:233], v[110:113]
	v_mfma_f32_16x16x32_bf16 v[106:109], v[186:189], v[226:229], v[106:109]
	v_mfma_f32_16x16x32_bf16 v[106:109], v[190:193], v[230:233], v[106:109]
	v_mfma_f32_16x16x32_bf16 v[102:105], v[162:165], v[234:237], v[102:105]
	v_mfma_f32_16x16x32_bf16 v[102:105], v[182:185], v[238:241], v[102:105]
	s_waitcnt lgkmcnt(0)
	v_mfma_f32_16x16x32_bf16 v[98:101], v[186:189], v[234:237], v[98:101]
	v_mfma_f32_16x16x32_bf16 v[98:101], v[190:193], v[238:241], v[98:101]
	v_mfma_f32_16x16x32_bf16 v[94:97], v[194:197], v[210:213], v[94:97]
	v_mfma_f32_16x16x32_bf16 v[94:97], v[198:201], v[214:217], v[94:97]
	v_mfma_f32_16x16x32_bf16 v[90:93], v[202:205], v[210:213], v[90:93]
	v_mfma_f32_16x16x32_bf16 v[90:93], v[206:209], v[214:217], v[90:93]
	v_mfma_f32_16x16x32_bf16 v[86:89], v[194:197], v[218:221], v[86:89]
	v_mfma_f32_16x16x32_bf16 v[86:89], v[198:201], v[222:225], v[86:89]
	v_mfma_f32_16x16x32_bf16 v[82:85], v[202:205], v[218:221], v[82:85]
	v_mfma_f32_16x16x32_bf16 v[82:85], v[206:209], v[222:225], v[82:85]
	v_mfma_f32_16x16x32_bf16 v[78:81], v[194:197], v[226:229], v[78:81]
	v_mfma_f32_16x16x32_bf16 v[78:81], v[198:201], v[230:233], v[78:81]
	v_mfma_f32_16x16x32_bf16 v[74:77], v[202:205], v[226:229], v[74:77]
	v_mfma_f32_16x16x32_bf16 v[74:77], v[206:209], v[230:233], v[74:77]
	v_mfma_f32_16x16x32_bf16 v[70:73], v[194:197], v[234:237], v[70:73]
	v_mfma_f32_16x16x32_bf16 v[70:73], v[198:201], v[238:241], v[70:73]
	v_mfma_f32_16x16x32_bf16 v[66:69], v[202:205], v[234:237], v[66:69]
	v_mfma_f32_16x16x32_bf16 v[66:69], v[206:209], v[238:241], v[66:69]
	s_barrier
	s_mov_b32 m0, s49
	ds_read_b128 v[210:213], v180 offset:49152
	ds_read_b128 v[214:217], v180 offset:50176
	ds_read_b128 v[218:221], v180 offset:51200
	ds_read_b128 v[222:225], v180 offset:52224
	ds_read_b128 v[226:229], v180 offset:53248
	ds_read_b128 v[230:233], v180 offset:54272
	ds_read_b128 v[234:237], v180 offset:55296
	ds_read_b128 v[238:241], v180 offset:56320
	buffer_load_dwordx4 v174, s[8:11], s28 offen lds
	s_mov_b32 m0, s50
	s_add_i32 s27, s27, 0x80080
	buffer_load_dwordx4 v176, s[8:11], s28 offen lds
	s_mov_b32 m0, s53
	s_nop 0
	buffer_load_dwordx4 v174, s[8:11], s27 offen lds
	s_mov_b32 m0, s54
	s_nop 0
	buffer_load_dwordx4 v176, s[8:11], s27 offen lds
	s_mov_b32 m0, s51
	s_nop 0
	buffer_load_dwordx4 v1, s[4:7], s26 offen lds
	s_mov_b32 m0, s52
	s_nop 0
	buffer_load_dwordx4 v175, s[4:7], s26 offen lds
	s_waitcnt vmcnt(8)
	s_waitcnt lgkmcnt(0)
	s_barrier
	s_waitcnt lgkmcnt(7)
	v_mfma_f32_16x16x32_bf16 v[62:65], v[162:165], v[210:213], v[62:65]
	v_mfma_f32_16x16x32_bf16 v[62:65], v[182:185], v[214:217], v[62:65]
	s_waitcnt lgkmcnt(5)
	v_mfma_f32_16x16x32_bf16 v[58:61], v[186:189], v[210:213], v[58:61]
	v_mfma_f32_16x16x32_bf16 v[58:61], v[190:193], v[214:217], v[58:61]
	s_waitcnt lgkmcnt(3)
	v_mfma_f32_16x16x32_bf16 v[54:57], v[162:165], v[218:221], v[54:57]
	v_mfma_f32_16x16x32_bf16 v[54:57], v[182:185], v[222:225], v[54:57]
	s_waitcnt lgkmcnt(1)
	v_mfma_f32_16x16x32_bf16 v[50:53], v[186:189], v[218:221], v[50:53]
	v_mfma_f32_16x16x32_bf16 v[50:53], v[190:193], v[222:225], v[50:53]
	v_mfma_f32_16x16x32_bf16 v[46:49], v[162:165], v[226:229], v[46:49]
	v_mfma_f32_16x16x32_bf16 v[46:49], v[182:185], v[230:233], v[46:49]
	v_mfma_f32_16x16x32_bf16 v[42:45], v[186:189], v[226:229], v[42:45]
	v_mfma_f32_16x16x32_bf16 v[42:45], v[190:193], v[230:233], v[42:45]
	v_mfma_f32_16x16x32_bf16 v[38:41], v[162:165], v[234:237], v[38:41]
	v_mfma_f32_16x16x32_bf16 v[38:41], v[182:185], v[238:241], v[38:41]
	s_waitcnt lgkmcnt(0)
	v_mfma_f32_16x16x32_bf16 v[34:37], v[186:189], v[234:237], v[34:37]
	v_mfma_f32_16x16x32_bf16 v[34:37], v[190:193], v[238:241], v[34:37]
	v_mfma_f32_16x16x32_bf16 v[30:33], v[194:197], v[210:213], v[30:33]
	v_mfma_f32_16x16x32_bf16 v[30:33], v[198:201], v[214:217], v[30:33]
	v_mfma_f32_16x16x32_bf16 v[26:29], v[202:205], v[210:213], v[26:29]
	v_mfma_f32_16x16x32_bf16 v[26:29], v[206:209], v[214:217], v[26:29]
	v_mfma_f32_16x16x32_bf16 v[22:25], v[194:197], v[218:221], v[22:25]
	v_mfma_f32_16x16x32_bf16 v[22:25], v[198:201], v[222:225], v[22:25]
	v_mfma_f32_16x16x32_bf16 v[18:21], v[202:205], v[218:221], v[18:21]
	v_mfma_f32_16x16x32_bf16 v[18:21], v[206:209], v[222:225], v[18:21]
	v_mfma_f32_16x16x32_bf16 v[14:17], v[194:197], v[226:229], v[14:17]
	v_mfma_f32_16x16x32_bf16 v[14:17], v[198:201], v[230:233], v[14:17]
	v_mfma_f32_16x16x32_bf16 v[10:13], v[202:205], v[226:229], v[10:13]
	v_mfma_f32_16x16x32_bf16 v[10:13], v[206:209], v[230:233], v[10:13]
	v_mfma_f32_16x16x32_bf16 v[6:9], v[194:197], v[234:237], v[6:9]
	v_mfma_f32_16x16x32_bf16 v[6:9], v[198:201], v[238:241], v[6:9]
	v_mfma_f32_16x16x32_bf16 v[2:5], v[202:205], v[234:237], v[2:5]
	v_mfma_f32_16x16x32_bf16 v[2:5], v[206:209], v[238:241], v[2:5]
	s_barrier
	s_add_i32 s10, s65, 2
	s_addk_i32 s64, 0x100
	s_cmp_gt_u32 s65, 29
	s_cbranch_scc1 .LBB0_910
	s_mov_b32 s65, s10
	s_branch .LBB0_869

.LBB0_1029:
	v_add_u32_e32 v152, 0x10000, v138
	v_add_u32_e32 v168, 0x14000, v138
	ds_read_b128 v[140:143], v152
	ds_read_b128 v[144:147], v152 offset:1024
	ds_read_b128 v[148:151], v152 offset:2048
	ds_read_b128 v[152:155], v152 offset:3072
	ds_read_b128 v[156:159], v168
	ds_read_b128 v[160:163], v168 offset:1024
	ds_read_b128 v[164:167], v168 offset:2048
	ds_read_b128 v[168:171], v168 offset:3072
	s_add_i32 s10, s30, s50
	s_add_i32 s51, s25, s50
	s_add_i32 s11, s10, 0x4000
	s_addk_i32 s51, 0x4000
	s_cmp_eq_u32 s50, 0
	s_cselect_b32 s53, s47, s11
	s_cselect_b32 s52, s48, s51
	s_or_b32 s51, s53, 0x80
	s_add_i32 s10, s10, 0x203f80
	s_mov_b32 m0, s41
	ds_read_b128 v[172:175], v139
	ds_read_b128 v[176:179], v139 offset:1024
	ds_read_b128 v[180:183], v139 offset:2048
	ds_read_b128 v[184:187], v139 offset:3072
	ds_read_b128 v[188:191], v139 offset:4096
	ds_read_b128 v[192:195], v139 offset:5120
	ds_read_b128 v[196:199], v139 offset:6144
	ds_read_b128 v[200:203], v139 offset:7168
	buffer_load_dwordx4 v134, s[4:7], s10 offen lds
	s_mov_b32 m0, s42
	s_nop 0
	buffer_load_dwordx4 v136, s[4:7], s10 offen lds
	s_waitcnt vmcnt(8)
	s_waitcnt lgkmcnt(0)
	s_barrier
	s_waitcnt lgkmcnt(7)
	v_mfma_f32_16x16x32_bf16 v[126:129], v[140:143], v[172:175], v[126:129]
	v_mfma_f32_16x16x32_bf16 v[126:129], v[144:147], v[176:179], v[126:129]
	s_waitcnt lgkmcnt(5)
	v_mfma_f32_16x16x32_bf16 v[122:125], v[148:151], v[172:175], v[122:125]
	v_mfma_f32_16x16x32_bf16 v[122:125], v[152:155], v[176:179], v[122:125]
	s_waitcnt lgkmcnt(3)
	v_mfma_f32_16x16x32_bf16 v[114:117], v[140:143], v[180:183], v[114:117]
	v_mfma_f32_16x16x32_bf16 v[114:117], v[144:147], v[184:187], v[114:117]
	s_waitcnt lgkmcnt(1)
	v_mfma_f32_16x16x32_bf16 v[106:109], v[148:151], v[180:183], v[106:109]
	v_mfma_f32_16x16x32_bf16 v[106:109], v[152:155], v[184:187], v[106:109]
	v_mfma_f32_16x16x32_bf16 v[98:101], v[140:143], v[188:191], v[98:101]
	v_mfma_f32_16x16x32_bf16 v[98:101], v[144:147], v[192:195], v[98:101]
	v_mfma_f32_16x16x32_bf16 v[90:93], v[148:151], v[188:191], v[90:93]
	v_mfma_f32_16x16x32_bf16 v[90:93], v[152:155], v[192:195], v[90:93]
	v_mfma_f32_16x16x32_bf16 v[82:85], v[140:143], v[196:199], v[82:85]
	v_mfma_f32_16x16x32_bf16 v[82:85], v[144:147], v[200:203], v[82:85]
	s_waitcnt lgkmcnt(0)
	v_mfma_f32_16x16x32_bf16 v[74:77], v[148:151], v[196:199], v[74:77]
	v_mfma_f32_16x16x32_bf16 v[74:77], v[152:155], v[200:203], v[74:77]
	v_mfma_f32_16x16x32_bf16 v[118:121], v[156:159], v[172:175], v[118:121]
	v_mfma_f32_16x16x32_bf16 v[118:121], v[160:163], v[176:179], v[118:121]
	v_mfma_f32_16x16x32_bf16 v[110:113], v[164:167], v[172:175], v[110:113]
	v_mfma_f32_16x16x32_bf16 v[110:113], v[168:171], v[176:179], v[110:113]
	v_mfma_f32_16x16x32_bf16 v[102:105], v[156:159], v[180:183], v[102:105]
	v_mfma_f32_16x16x32_bf16 v[102:105], v[160:163], v[184:187], v[102:105]
	v_mfma_f32_16x16x32_bf16 v[94:97], v[164:167], v[180:183], v[94:97]
	v_mfma_f32_16x16x32_bf16 v[94:97], v[168:171], v[184:187], v[94:97]
	v_mfma_f32_16x16x32_bf16 v[86:89], v[156:159], v[188:191], v[86:89]
	v_mfma_f32_16x16x32_bf16 v[86:89], v[160:163], v[192:195], v[86:89]
	v_mfma_f32_16x16x32_bf16 v[78:81], v[164:167], v[188:191], v[78:81]
	v_mfma_f32_16x16x32_bf16 v[78:81], v[168:171], v[192:195], v[78:81]
	v_mfma_f32_16x16x32_bf16 v[70:73], v[156:159], v[196:199], v[70:73]
	v_mfma_f32_16x16x32_bf16 v[70:73], v[160:163], v[200:203], v[70:73]
	v_mfma_f32_16x16x32_bf16 v[66:69], v[164:167], v[196:199], v[66:69]
	v_mfma_f32_16x16x32_bf16 v[66:69], v[168:171], v[200:203], v[66:69]
	s_barrier
	s_mov_b32 m0, s24
	s_mov_b32 s10, s6
	s_mov_b32 s11, s7
	ds_read_b128 v[172:175], v139 offset:16384
	ds_read_b128 v[176:179], v139 offset:17408
	ds_read_b128 v[180:183], v139 offset:18432
	ds_read_b128 v[184:187], v139 offset:19456
	ds_read_b128 v[188:191], v139 offset:20480
	ds_read_b128 v[192:195], v139 offset:21504
	ds_read_b128 v[196:199], v139 offset:22528
	ds_read_b128 v[200:203], v139 offset:23552
	buffer_load_dwordx4 v135, s[8:11], s52 offen lds
	s_mov_b32 m0, s26
	s_add_i32 s54, s52, 0x200000
	buffer_load_dwordx4 v137, s[8:11], s52 offen lds
	s_mov_b32 m0, s27
	s_nop 0
	buffer_load_dwordx4 v135, s[8:11], s54 offen lds
	s_mov_b32 m0, s28
	s_nop 0
	buffer_load_dwordx4 v137, s[8:11], s54 offen lds
	s_mov_b32 m0, s23
	s_nop 0
	buffer_load_dwordx4 v134, s[4:7], s53 offen lds
	s_mov_b32 m0, s29
	s_nop 0
	buffer_load_dwordx4 v136, s[4:7], s53 offen lds
	s_waitcnt vmcnt(8)
	s_waitcnt lgkmcnt(0)
	s_barrier
	s_waitcnt lgkmcnt(7)
	v_mfma_f32_16x16x32_bf16 v[62:65], v[140:143], v[172:175], v[62:65]
	v_mfma_f32_16x16x32_bf16 v[62:65], v[144:147], v[176:179], v[62:65]
	s_waitcnt lgkmcnt(5)
	v_mfma_f32_16x16x32_bf16 v[58:61], v[148:151], v[172:175], v[58:61]
	v_mfma_f32_16x16x32_bf16 v[58:61], v[152:155], v[176:179], v[58:61]
	s_waitcnt lgkmcnt(3)
	v_mfma_f32_16x16x32_bf16 v[50:53], v[140:143], v[180:183], v[50:53]
	v_mfma_f32_16x16x32_bf16 v[50:53], v[144:147], v[184:187], v[50:53]
	s_waitcnt lgkmcnt(1)
	v_mfma_f32_16x16x32_bf16 v[42:45], v[148:151], v[180:183], v[42:45]
	v_mfma_f32_16x16x32_bf16 v[42:45], v[152:155], v[184:187], v[42:45]
	v_mfma_f32_16x16x32_bf16 v[34:37], v[140:143], v[188:191], v[34:37]
	v_mfma_f32_16x16x32_bf16 v[34:37], v[144:147], v[192:195], v[34:37]
	v_mfma_f32_16x16x32_bf16 v[26:29], v[148:151], v[188:191], v[26:29]
	v_mfma_f32_16x16x32_bf16 v[26:29], v[152:155], v[192:195], v[26:29]
	v_mfma_f32_16x16x32_bf16 v[18:21], v[140:143], v[196:199], v[18:21]
	v_mfma_f32_16x16x32_bf16 v[18:21], v[144:147], v[200:203], v[18:21]
	s_waitcnt lgkmcnt(0)
	v_mfma_f32_16x16x32_bf16 v[10:13], v[148:151], v[196:199], v[10:13]
	v_mfma_f32_16x16x32_bf16 v[10:13], v[152:155], v[200:203], v[10:13]
	v_mfma_f32_16x16x32_bf16 v[54:57], v[156:159], v[172:175], v[54:57]
	v_mfma_f32_16x16x32_bf16 v[54:57], v[160:163], v[176:179], v[54:57]
	v_mfma_f32_16x16x32_bf16 v[46:49], v[164:167], v[172:175], v[46:49]
	v_mfma_f32_16x16x32_bf16 v[46:49], v[168:171], v[176:179], v[46:49]
	v_mfma_f32_16x16x32_bf16 v[38:41], v[156:159], v[180:183], v[38:41]
	v_mfma_f32_16x16x32_bf16 v[38:41], v[160:163], v[184:187], v[38:41]
	v_mfma_f32_16x16x32_bf16 v[30:33], v[164:167], v[180:183], v[30:33]
	v_mfma_f32_16x16x32_bf16 v[30:33], v[168:171], v[184:187], v[30:33]
	v_mfma_f32_16x16x32_bf16 v[22:25], v[156:159], v[188:191], v[22:25]
	v_mfma_f32_16x16x32_bf16 v[22:25], v[160:163], v[192:195], v[22:25]
	v_mfma_f32_16x16x32_bf16 v[14:17], v[164:167], v[188:191], v[14:17]
	v_mfma_f32_16x16x32_bf16 v[14:17], v[168:171], v[192:195], v[14:17]
	v_mfma_f32_16x16x32_bf16 v[6:9], v[156:159], v[196:199], v[6:9]
	v_mfma_f32_16x16x32_bf16 v[6:9], v[160:163], v[200:203], v[6:9]
	v_mfma_f32_16x16x32_bf16 v[2:5], v[164:167], v[196:199], v[2:5]
	v_mfma_f32_16x16x32_bf16 v[2:5], v[168:171], v[200:203], v[2:5]
	s_barrier
	v_add_u32_e32 v152, 0x18000, v138
	v_add_u32_e32 v168, 0x1c000, v138
	ds_read_b128 v[140:143], v152
	ds_read_b128 v[144:147], v152 offset:1024
	ds_read_b128 v[148:151], v152 offset:2048
	ds_read_b128 v[152:155], v152 offset:3072
	ds_read_b128 v[156:159], v168
	ds_read_b128 v[160:163], v168 offset:1024
	ds_read_b128 v[164:167], v168 offset:2048
	ds_read_b128 v[168:171], v168 offset:3072
	s_add_i32 s53, s53, 0x200000
	s_mov_b32 m0, s31
	ds_read_b128 v[172:175], v139 offset:32768
	ds_read_b128 v[176:179], v139 offset:33792
	ds_read_b128 v[180:183], v139 offset:34816
	ds_read_b128 v[184:187], v139 offset:35840
	ds_read_b128 v[188:191], v139 offset:36864
	ds_read_b128 v[192:195], v139 offset:37888
	ds_read_b128 v[196:199], v139 offset:38912
	ds_read_b128 v[200:203], v139 offset:39936
	buffer_load_dwordx4 v134, s[4:7], s53 offen lds
	s_mov_b32 m0, s33
	s_nop 0
	buffer_load_dwordx4 v136, s[4:7], s53 offen lds
	s_waitcnt vmcnt(8)
	s_waitcnt lgkmcnt(0)
	s_barrier
	s_waitcnt lgkmcnt(7)
	v_mfma_f32_16x16x32_bf16 v[126:129], v[140:143], v[172:175], v[126:129]
	v_mfma_f32_16x16x32_bf16 v[126:129], v[144:147], v[176:179], v[126:129]
	s_waitcnt lgkmcnt(5)
	v_mfma_f32_16x16x32_bf16 v[122:125], v[148:151], v[172:175], v[122:125]
	v_mfma_f32_16x16x32_bf16 v[122:125], v[152:155], v[176:179], v[122:125]
	s_waitcnt lgkmcnt(3)
	v_mfma_f32_16x16x32_bf16 v[114:117], v[140:143], v[180:183], v[114:117]
	v_mfma_f32_16x16x32_bf16 v[114:117], v[144:147], v[184:187], v[114:117]
	s_waitcnt lgkmcnt(1)
	v_mfma_f32_16x16x32_bf16 v[106:109], v[148:151], v[180:183], v[106:109]
	v_mfma_f32_16x16x32_bf16 v[106:109], v[152:155], v[184:187], v[106:109]
	v_mfma_f32_16x16x32_bf16 v[98:101], v[140:143], v[188:191], v[98:101]
	v_mfma_f32_16x16x32_bf16 v[98:101], v[144:147], v[192:195], v[98:101]
	v_mfma_f32_16x16x32_bf16 v[90:93], v[148:151], v[188:191], v[90:93]
	v_mfma_f32_16x16x32_bf16 v[90:93], v[152:155], v[192:195], v[90:93]
	v_mfma_f32_16x16x32_bf16 v[82:85], v[140:143], v[196:199], v[82:85]
	v_mfma_f32_16x16x32_bf16 v[82:85], v[144:147], v[200:203], v[82:85]
	s_waitcnt lgkmcnt(0)
	v_mfma_f32_16x16x32_bf16 v[74:77], v[148:151], v[196:199], v[74:77]
	v_mfma_f32_16x16x32_bf16 v[74:77], v[152:155], v[200:203], v[74:77]
	v_mfma_f32_16x16x32_bf16 v[118:121], v[156:159], v[172:175], v[118:121]
	v_mfma_f32_16x16x32_bf16 v[118:121], v[160:163], v[176:179], v[118:121]
	v_mfma_f32_16x16x32_bf16 v[110:113], v[164:167], v[172:175], v[110:113]
	v_mfma_f32_16x16x32_bf16 v[110:113], v[168:171], v[176:179], v[110:113]
	v_mfma_f32_16x16x32_bf16 v[102:105], v[156:159], v[180:183], v[102:105]
	v_mfma_f32_16x16x32_bf16 v[102:105], v[160:163], v[184:187], v[102:105]
	v_mfma_f32_16x16x32_bf16 v[94:97], v[164:167], v[180:183], v[94:97]
	v_mfma_f32_16x16x32_bf16 v[94:97], v[168:171], v[184:187], v[94:97]
	v_mfma_f32_16x16x32_bf16 v[86:89], v[156:159], v[188:191], v[86:89]
	v_mfma_f32_16x16x32_bf16 v[86:89], v[160:163], v[192:195], v[86:89]
	v_mfma_f32_16x16x32_bf16 v[78:81], v[164:167], v[188:191], v[78:81]
	v_mfma_f32_16x16x32_bf16 v[78:81], v[168:171], v[192:195], v[78:81]
	v_mfma_f32_16x16x32_bf16 v[70:73], v[156:159], v[196:199], v[70:73]
	v_mfma_f32_16x16x32_bf16 v[70:73], v[160:163], v[200:203], v[70:73]
	v_mfma_f32_16x16x32_bf16 v[66:69], v[164:167], v[196:199], v[66:69]
	v_mfma_f32_16x16x32_bf16 v[66:69], v[168:171], v[200:203], v[66:69]
	s_barrier
	s_mov_b32 m0, s34
	s_or_b32 s53, s52, 0x80
	ds_read_b128 v[172:175], v139 offset:49152
	ds_read_b128 v[176:179], v139 offset:50176
	ds_read_b128 v[180:183], v139 offset:51200
	ds_read_b128 v[184:187], v139 offset:52224
	ds_read_b128 v[188:191], v139 offset:53248
	ds_read_b128 v[192:195], v139 offset:54272
	ds_read_b128 v[196:199], v139 offset:55296
	ds_read_b128 v[200:203], v139 offset:56320
	buffer_load_dwordx4 v135, s[8:11], s53 offen lds
	s_mov_b32 m0, s35
	s_add_i32 s52, s52, 0x200080
	buffer_load_dwordx4 v137, s[8:11], s53 offen lds
	s_mov_b32 m0, s39
	s_nop 0
	buffer_load_dwordx4 v135, s[8:11], s52 offen lds
	s_mov_b32 m0, s40
	s_nop 0
	buffer_load_dwordx4 v137, s[8:11], s52 offen lds
	s_mov_b32 m0, s37
	s_nop 0
	buffer_load_dwordx4 v134, s[4:7], s51 offen lds
	s_mov_b32 m0, s38
	s_nop 0
	buffer_load_dwordx4 v136, s[4:7], s51 offen lds
	s_waitcnt vmcnt(8)
	s_waitcnt lgkmcnt(0)
	s_barrier
	s_waitcnt lgkmcnt(7)
	v_mfma_f32_16x16x32_bf16 v[62:65], v[140:143], v[172:175], v[62:65]
	v_mfma_f32_16x16x32_bf16 v[62:65], v[144:147], v[176:179], v[62:65]
	s_waitcnt lgkmcnt(5)
	v_mfma_f32_16x16x32_bf16 v[58:61], v[148:151], v[172:175], v[58:61]
	v_mfma_f32_16x16x32_bf16 v[58:61], v[152:155], v[176:179], v[58:61]
	s_waitcnt lgkmcnt(3)
	v_mfma_f32_16x16x32_bf16 v[50:53], v[140:143], v[180:183], v[50:53]
	v_mfma_f32_16x16x32_bf16 v[50:53], v[144:147], v[184:187], v[50:53]
	s_waitcnt lgkmcnt(1)
	v_mfma_f32_16x16x32_bf16 v[42:45], v[148:151], v[180:183], v[42:45]
	v_mfma_f32_16x16x32_bf16 v[42:45], v[152:155], v[184:187], v[42:45]
	v_mfma_f32_16x16x32_bf16 v[34:37], v[140:143], v[188:191], v[34:37]
	v_mfma_f32_16x16x32_bf16 v[34:37], v[144:147], v[192:195], v[34:37]
	v_mfma_f32_16x16x32_bf16 v[26:29], v[148:151], v[188:191], v[26:29]
	v_mfma_f32_16x16x32_bf16 v[26:29], v[152:155], v[192:195], v[26:29]
	v_mfma_f32_16x16x32_bf16 v[18:21], v[140:143], v[196:199], v[18:21]
	v_mfma_f32_16x16x32_bf16 v[18:21], v[144:147], v[200:203], v[18:21]
	s_waitcnt lgkmcnt(0)
	v_mfma_f32_16x16x32_bf16 v[10:13], v[148:151], v[196:199], v[10:13]
	v_mfma_f32_16x16x32_bf16 v[10:13], v[152:155], v[200:203], v[10:13]
	v_mfma_f32_16x16x32_bf16 v[54:57], v[156:159], v[172:175], v[54:57]
	v_mfma_f32_16x16x32_bf16 v[54:57], v[160:163], v[176:179], v[54:57]
	v_mfma_f32_16x16x32_bf16 v[46:49], v[164:167], v[172:175], v[46:49]
	v_mfma_f32_16x16x32_bf16 v[46:49], v[168:171], v[176:179], v[46:49]
	v_mfma_f32_16x16x32_bf16 v[38:41], v[156:159], v[180:183], v[38:41]
	v_mfma_f32_16x16x32_bf16 v[38:41], v[160:163], v[184:187], v[38:41]
	v_mfma_f32_16x16x32_bf16 v[30:33], v[164:167], v[180:183], v[30:33]
	v_mfma_f32_16x16x32_bf16 v[30:33], v[168:171], v[184:187], v[30:33]
	v_mfma_f32_16x16x32_bf16 v[22:25], v[156:159], v[188:191], v[22:25]
	v_mfma_f32_16x16x32_bf16 v[22:25], v[160:163], v[192:195], v[22:25]
	v_mfma_f32_16x16x32_bf16 v[14:17], v[164:167], v[188:191], v[14:17]
	v_mfma_f32_16x16x32_bf16 v[14:17], v[168:171], v[192:195], v[14:17]
	v_mfma_f32_16x16x32_bf16 v[6:9], v[156:159], v[196:199], v[6:9]
	v_mfma_f32_16x16x32_bf16 v[6:9], v[160:163], v[200:203], v[6:9]
	v_mfma_f32_16x16x32_bf16 v[2:5], v[164:167], v[196:199], v[2:5]
	v_mfma_f32_16x16x32_bf16 v[2:5], v[168:171], v[200:203], v[2:5]
	s_barrier
	s_add_i32 s49, s49, 2
	s_addk_i32 s50, 0x100
	s_cmpk_gt_u32 s49, 0x7d
	s_cbranch_scc0 .LBB0_1029
	s_andn2_b64 vcc, exec, s[2:3]
	s_cbranch_vccnz .LBB0_1021
	v_mov_b32_e32 v2, 0
	s_mov_b32 s17, s44
	s_mov_b32 s14, s45
	s_mov_b32 s25, s46
	s_mov_b32 s30, s13
	s_mov_b32 s43, s12
	v_mov_b32_e32 v3, v2
	v_mov_b32_e32 v4, v2
	v_mov_b32_e32 v5, v2
	v_mov_b32_e32 v6, v2
	v_mov_b32_e32 v7, v2
	v_mov_b32_e32 v8, v2
	v_mov_b32_e32 v9, v2
	v_mov_b32_e32 v14, v2
	v_mov_b32_e32 v15, v2
	v_mov_b32_e32 v16, v2
	v_mov_b32_e32 v17, v2
	v_mov_b32_e32 v22, v2
	v_mov_b32_e32 v23, v2
	v_mov_b32_e32 v24, v2
	v_mov_b32_e32 v25, v2
	v_mov_b32_e32 v30, v2
	v_mov_b32_e32 v31, v2
	v_mov_b32_e32 v32, v2
	v_mov_b32_e32 v33, v2
	v_mov_b32_e32 v38, v2
	v_mov_b32_e32 v39, v2
	v_mov_b32_e32 v40, v2
	v_mov_b32_e32 v41, v2
	v_mov_b32_e32 v46, v2
	v_mov_b32_e32 v47, v2
	v_mov_b32_e32 v48, v2
	v_mov_b32_e32 v49, v2
	v_mov_b32_e32 v54, v2
	v_mov_b32_e32 v55, v2
	v_mov_b32_e32 v56, v2
	v_mov_b32_e32 v57, v2
	v_mov_b32_e32 v10, v2
	v_mov_b32_e32 v11, v2
	v_mov_b32_e32 v12, v2
	v_mov_b32_e32 v13, v2
	v_mov_b32_e32 v18, v2
	v_mov_b32_e32 v19, v2
	v_mov_b32_e32 v20, v2
	v_mov_b32_e32 v21, v2
	v_mov_b32_e32 v26, v2
	v_mov_b32_e32 v27, v2
	v_mov_b32_e32 v28, v2
	v_mov_b32_e32 v29, v2
	v_mov_b32_e32 v34, v2
	v_mov_b32_e32 v35, v2
	v_mov_b32_e32 v36, v2
	v_mov_b32_e32 v37, v2
	v_mov_b32_e32 v42, v2
	v_mov_b32_e32 v43, v2
	v_mov_b32_e32 v44, v2
	v_mov_b32_e32 v45, v2
	v_mov_b32_e32 v50, v2
	v_mov_b32_e32 v51, v2
	v_mov_b32_e32 v52, v2
	v_mov_b32_e32 v53, v2
	v_mov_b32_e32 v58, v2
	v_mov_b32_e32 v59, v2
	v_mov_b32_e32 v60, v2
	v_mov_b32_e32 v61, v2
	v_mov_b32_e32 v62, v2
	v_mov_b32_e32 v63, v2
	v_mov_b32_e32 v64, v2
	v_mov_b32_e32 v65, v2
	v_mov_b32_e32 v66, v2
	v_mov_b32_e32 v67, v2
	v_mov_b32_e32 v68, v2
	v_mov_b32_e32 v69, v2
	v_mov_b32_e32 v70, v2
	v_mov_b32_e32 v71, v2
	v_mov_b32_e32 v72, v2
	v_mov_b32_e32 v73, v2
	v_mov_b32_e32 v78, v2
	v_mov_b32_e32 v79, v2
	v_mov_b32_e32 v80, v2
	v_mov_b32_e32 v81, v2
	v_mov_b32_e32 v86, v2
	v_mov_b32_e32 v87, v2
	v_mov_b32_e32 v88, v2
	v_mov_b32_e32 v89, v2
	v_mov_b32_e32 v94, v2
	v_mov_b32_e32 v95, v2
	v_mov_b32_e32 v96, v2
	v_mov_b32_e32 v97, v2
	v_mov_b32_e32 v102, v2
	v_mov_b32_e32 v103, v2
	v_mov_b32_e32 v104, v2
	v_mov_b32_e32 v105, v2
	v_mov_b32_e32 v110, v2
	v_mov_b32_e32 v111, v2
	v_mov_b32_e32 v112, v2
	v_mov_b32_e32 v113, v2
	v_mov_b32_e32 v118, v2
	v_mov_b32_e32 v119, v2
	v_mov_b32_e32 v120, v2
	v_mov_b32_e32 v121, v2
	v_mov_b32_e32 v74, v2
	v_mov_b32_e32 v75, v2
	v_mov_b32_e32 v76, v2
	v_mov_b32_e32 v77, v2
	v_mov_b32_e32 v82, v2
	v_mov_b32_e32 v83, v2
	v_mov_b32_e32 v84, v2
	v_mov_b32_e32 v85, v2
	v_mov_b32_e32 v90, v2
	v_mov_b32_e32 v91, v2
	v_mov_b32_e32 v92, v2
	v_mov_b32_e32 v93, v2
	v_mov_b32_e32 v98, v2
	v_mov_b32_e32 v99, v2
	v_mov_b32_e32 v100, v2
	v_mov_b32_e32 v101, v2
	v_mov_b32_e32 v106, v2
	v_mov_b32_e32 v107, v2
	v_mov_b32_e32 v108, v2
	v_mov_b32_e32 v109, v2
	v_mov_b32_e32 v114, v2
	v_mov_b32_e32 v115, v2
	v_mov_b32_e32 v116, v2
	v_mov_b32_e32 v117, v2
	v_mov_b32_e32 v122, v2
	v_mov_b32_e32 v123, v2
	v_mov_b32_e32 v124, v2
	v_mov_b32_e32 v125, v2
	v_mov_b32_e32 v126, v2
	v_mov_b32_e32 v127, v2
	v_mov_b32_e32 v128, v2
	v_mov_b32_e32 v129, v2
	s_branch .LBB0_1021
